# rmsnorm loops (prologue, final): g vectors hoisted out of the row loop, removing per-row store-ack waits
# speedup vs baseline: 1.0079x; 1.0058x over previous
; __device__ __forceinline__ void row_store_norm_bf16(bf16* __restrict__ o, const float* __restrict__ g, int lane, const float (&v)[32], float r) {
; #pragma unroll
;     for (int cch = 0; cch < 4; ++cch) { const f32x4 ga = *(const f32x4*)(g + cch * 512 + lane * 8), gb = *(const f32x4*)(g + cch * 512 + lane * 8 + 4); float f[8];
; __device__ __forceinline__ void ph_prologue(const Ctx& c) {
;     ...
;         const int nrow = bal ? (heavy ? 6 : 10) : (T_ + c.G * NWAVE - 1) / (c.G * NWAVE);
;         const int row0 = bal ? (heavy ? (c.bid * NWAVE + c.wave) * 6 : 128 * NWAVE * 6 + ((c.bid - 128) * NWAVE + c.wave) * 10) : (c.bid * NWAVE + c.wave) * nrow;
;         for (int i = 0; i < nrow; ++i) { const int row = row0 + i; if (row >= T_) break;
;             float v[32]; row_load32(c.in[0] + (size_t)row * D_, c.lane, v);
;             const float r = row_rstd(v);
;             row_store_norm_bf16(WSP(bf16, WS_HB) + (size_t)row * D_, c.in[1], c.lane, v, r);
;         }
.LBB0_165:
	s_cmp_lt_i32 s3, 1
	s_cbranch_scc1 .LBB0_170
	v_ashrrev_i32_e32 v1, 31, v0
	v_readlane_b32 s8, v254, 11
	v_lshlrev_b64 v[2:3], 2, v[0:1]
	v_readlane_b32 s10, v254, 13
	v_readlane_b32 s11, v254, 14
	s_mov_b64 s[6:7], 0x1800
	s_ashr_i32 s1, s0, 31
	v_lshl_add_u64 v[10:11], s[10:11], 0, v[2:3]
	v_lshl_add_u64 v[14:15], v[10:11], 0, s[6:7]
	s_lshl_b64 s[6:7], s[0:1], 13
	v_readlane_b32 s9, v254, 12
	s_add_u32 s6, s8, s6
	s_addc_u32 s7, s9, s7
	v_lshl_add_u64 v[2:3], s[6:7], 0, v[2:3]
	s_lshl_b64 s[6:7], s[0:1], 12
	s_add_u32 s6, s46, s6
	s_addc_u32 s7, s47, s7
	v_lshl_add_u64 v[0:1], v[0:1], 1, s[6:7]
	s_mov_b64 s[6:7], 0x33500000
	v_lshl_add_u64 v[18:19], v[0:1], 0, s[6:7]
	v_mbcnt_lo_u32_b32 v0, -1, 0
	v_mbcnt_hi_u32_b32 v20, -1, v0
	s_mov_b64 s[4:5], 0x1000
	v_and_b32_e32 v0, 64, v20
	v_lshl_add_u64 v[12:13], v[10:11], 0, s[4:5]
	v_lshl_add_u64 v[16:17], v[2:3], 0, s[4:5]
	v_mov_b32_e32 v9, 0x358637bd
	s_mov_b32 s1, 0x800000
	s_mov_b64 s[6:7], 0x2000
	v_add_u32_e32 v21, 64, v0
	v_xor_b32_e32 v22, 32, v20
	v_xor_b32_e32 v23, 16, v20
	v_xor_b32_e32 v24, 8, v20
	v_xor_b32_e32 v25, 4, v20
	v_xor_b32_e32 v26, 2, v20
	v_xor_b32_e32 v27, 1, v20
	v_readlane_b32 s12, v254, 15
	v_readlane_b32 s13, v254, 16
	v_readlane_b32 s14, v254, 17
	v_readlane_b32 s15, v254, 18
	v_readlane_b32 s16, v254, 19
	v_readlane_b32 s17, v254, 20
	v_readlane_b32 s18, v254, 21
	v_readlane_b32 s19, v254, 22
	v_readlane_b32 s20, v254, 23
	v_readlane_b32 s21, v254, 24
	v_readlane_b32 s22, v254, 25
	v_readlane_b32 s23, v254, 26
	global_load_dwordx4 v[52:55], v[10:11], off offset:16
	global_load_dwordx4 v[56:59], v[10:11], off
	global_load_dwordx4 v[112:115], v[10:11], off offset:2048
	global_load_dwordx4 v[116:119], v[10:11], off offset:2064
	global_load_dwordx4 v[120:123], v[12:13], off
	global_load_dwordx4 v[124:127], v[12:13], off offset:16
	global_load_dwordx4 v[128:131], v[14:15], off
	global_load_dwordx4 v[132:135], v[14:15], off offset:16
	s_waitcnt vmcnt(0)
	s_branch .LBB0_168

; __device__ __forceinline__ u32x4 pack8(const float (&v)[8]) { u32x4 w; w.x = pk2(v[0], v[1]); w.y = pk2(v[2], v[3]); w.z = pk2(v[4], v[5]); w.w = pk2(v[6], v[7]); return w; }
; __device__ __forceinline__ float row_rstd(const float (&v)[32]) {
;     float ss = 0.f;
; #pragma unroll
;     for (int j = 0; j < 32; ++j) ss += v[j] * v[j];
;     ss = wave_sum(ss);
;     return rsqrtf(ss * (1.0f / 2048.0f) + EPS);
; }
; __device__ __forceinline__ void row_store_norm_bf16(bf16* __restrict__ o, const float* __restrict__ g, int lane, const float (&v)[32], float r) {
; #pragma unroll
;     for (int cch = 0; cch < 4; ++cch) { const f32x4 ga = *(const f32x4*)(g + cch * 512 + lane * 8), gb = *(const f32x4*)(g + cch * 512 + lane * 8 + 4); float f[8];
; #pragma unroll
;         for (int j = 0; j < 4; ++j) { f[j] = v[cch * 8 + j] * r * ga[j]; f[4 + j] = v[cch * 8 + 4 + j] * r * gb[j]; }
;         *(u32x4*)(o + cch * 512 + lane * 8) = pack8(f); }
; __device__ __forceinline__ void ph_prologue(const Ctx& c) {
;     ...
;         for (int i = 0; i < nrow; ++i) { const int row = row0 + i; if (row >= T_) break;
;             float v[32]; row_load32(c.in[0] + (size_t)row * D_, c.lane, v);
;             const float r = row_rstd(v);
;             row_store_norm_bf16(WSP(bf16, WS_HB) + (size_t)row * D_, c.in[1], c.lane, v, r);
;         }
.LBB0_168:
	s_cmpk_gt_i32 s0, 0x3fff
	s_mov_b64 s[8:9], -1
	s_cbranch_scc1 .LBB0_167
	global_load_dwordx4 v[28:31], v[16:17], off offset:-4096
	global_load_dwordx4 v[0:3], v[16:17], off offset:2064
	global_load_dwordx4 v[32:35], v[16:17], off offset:-4080
	global_load_dwordx4 v[36:39], v[16:17], off offset:-2048
	global_load_dwordx4 v[40:43], v[16:17], off offset:-2032
	global_load_dwordx4 v[44:47], v[16:17], off
	global_load_dwordx4 v[48:51], v[16:17], off offset:16
	global_load_dwordx4 v[4:7], v[16:17], off offset:2048
	s_nop 0
	s_nop 0
	v_cmp_lt_i32_e32 vcc, v22, v21
	s_add_i32 s3, s3, -1
	s_add_i32 s0, s0, 1
	v_cndmask_b32_e32 v60, v20, v22, vcc
	v_lshlrev_b32_e32 v64, 2, v60
	v_cmp_lt_i32_e32 vcc, v23, v21
	s_cmp_eq_u32 s3, 0
	v_lshl_add_u64 v[16:17], v[16:17], 0, s[6:7]
	s_cselect_b64 s[8:9], -1, 0
	s_waitcnt vmcnt(7)
	v_mul_f32_e32 v65, v29, v29
	v_fmac_f32_e32 v65, v28, v28
	v_fmac_f32_e32 v65, v30, v30
	v_fmac_f32_e32 v65, v31, v31
	s_waitcnt vmcnt(5)
	v_fmac_f32_e32 v65, v32, v32
	v_fmac_f32_e32 v65, v33, v33
	v_fmac_f32_e32 v65, v34, v34
	v_fmac_f32_e32 v65, v35, v35
	s_waitcnt vmcnt(4)
	v_fmac_f32_e32 v65, v36, v36
	v_fmac_f32_e32 v65, v37, v37
	v_fmac_f32_e32 v65, v38, v38
	v_fmac_f32_e32 v65, v39, v39
	s_waitcnt vmcnt(3)
	v_fmac_f32_e32 v65, v40, v40
	v_fmac_f32_e32 v65, v41, v41
	v_fmac_f32_e32 v65, v42, v42
	v_fmac_f32_e32 v65, v43, v43
	s_waitcnt vmcnt(2)
	v_fmac_f32_e32 v65, v44, v44
	v_fmac_f32_e32 v65, v45, v45
	v_fmac_f32_e32 v65, v46, v46
	v_fmac_f32_e32 v65, v47, v47
	s_waitcnt vmcnt(1)
	v_fmac_f32_e32 v65, v48, v48
	v_fmac_f32_e32 v65, v49, v49
	v_fmac_f32_e32 v65, v50, v50
	v_fmac_f32_e32 v65, v51, v51
	s_waitcnt vmcnt(0)
	v_fmac_f32_e32 v65, v4, v4
	v_fmac_f32_e32 v65, v5, v5
	v_fmac_f32_e32 v65, v6, v6
	v_pk_mul_f32 v[62:63], v[0:1], v[0:1]
	v_fmac_f32_e32 v65, v7, v7
	v_add_f32_e32 v62, v62, v65
	v_pk_mul_f32 v[60:61], v[2:3], v[2:3]
	v_add_f32_e32 v62, v63, v62
	v_add_f32_e32 v60, v60, v62
	v_add_f32_e32 v60, v61, v60
	ds_bpermute_b32 v61, v64, v60
	v_cndmask_b32_e32 v62, v20, v23, vcc
	v_lshlrev_b32_e32 v62, 2, v62
	v_cmp_lt_i32_e32 vcc, v24, v21
	s_waitcnt lgkmcnt(0)
	v_add_f32_e32 v60, v60, v61
	ds_bpermute_b32 v61, v62, v60
	v_cndmask_b32_e32 v62, v20, v24, vcc
	v_lshlrev_b32_e32 v62, 2, v62
	v_cmp_lt_i32_e32 vcc, v25, v21
	s_waitcnt lgkmcnt(0)
	v_add_f32_e32 v60, v60, v61
	ds_bpermute_b32 v61, v62, v60
	v_cndmask_b32_e32 v62, v20, v25, vcc
	v_lshlrev_b32_e32 v62, 2, v62
	v_cmp_lt_i32_e32 vcc, v26, v21
	s_waitcnt lgkmcnt(0)
	v_add_f32_e32 v60, v60, v61
	ds_bpermute_b32 v61, v62, v60
	v_cndmask_b32_e32 v62, v20, v26, vcc
	v_lshlrev_b32_e32 v62, 2, v62
	v_cmp_lt_i32_e32 vcc, v27, v21
	s_waitcnt lgkmcnt(0)
	v_add_f32_e32 v60, v60, v61
	ds_bpermute_b32 v61, v62, v60
	v_cndmask_b32_e32 v62, v20, v27, vcc
	v_lshlrev_b32_e32 v62, 2, v62
	s_waitcnt lgkmcnt(0)
	v_add_f32_e32 v60, v60, v61
	ds_bpermute_b32 v61, v62, v60
	s_waitcnt lgkmcnt(0)
	v_add_f32_e32 v60, v60, v61
	v_fmamk_f32 v60, v60, 0x3a000000, v9
	v_mul_f32_e32 v61, 0x4b800000, v60
	v_cmp_gt_f32_e32 vcc, s1, v60
	s_nop 1
	v_cndmask_b32_e32 v60, v60, v61, vcc
	v_rsq_f32_e32 v60, v60
	s_nop 0
	v_mul_f32_e32 v61, 0x45800000, v60
	v_cndmask_b32_e32 v60, v60, v61, vcc
	v_pk_mul_f32 v[28:29], v[28:29], v[60:61] op_sel_hi:[1,0]
	v_pk_mul_f32 v[32:33], v[32:33], v[60:61] op_sel_hi:[1,0]
	v_pk_mul_f32 v[30:31], v[30:31], v[60:61] op_sel_hi:[1,0]
	v_pk_mul_f32 v[34:35], v[34:35], v[60:61] op_sel_hi:[1,0]
	s_nop 0
	v_pk_mul_f32 v[28:29], v[56:57], v[28:29]
	v_pk_mul_f32 v[32:33], v[52:53], v[32:33]
	v_pk_mul_f32 v[30:31], v[58:59], v[30:31]
	v_pk_mul_f32 v[34:35], v[54:55], v[34:35]
	v_cvt_pk_bf16_f32 v28, v28, v29
	v_cvt_pk_bf16_f32 v29, v30, v31
	v_cvt_pk_bf16_f32 v30, v32, v33
	v_cvt_pk_bf16_f32 v31, v34, v35
	global_store_dwordx4 v[18:19], v[28:31], off
	s_nop 0
	s_nop 0
	s_nop 0
	v_pk_mul_f32 v[36:37], v[36:37], v[60:61] op_sel_hi:[1,0]
	v_pk_mul_f32 v[40:41], v[40:41], v[60:61] op_sel_hi:[1,0]
	v_pk_mul_f32 v[38:39], v[38:39], v[60:61] op_sel_hi:[1,0]
	v_pk_mul_f32 v[42:43], v[42:43], v[60:61] op_sel_hi:[1,0]
	v_pk_mul_f32 v[4:5], v[4:5], v[60:61] op_sel_hi:[1,0]
	v_pk_mul_f32 v[0:1], v[0:1], v[60:61] op_sel_hi:[1,0]
	v_pk_mul_f32 v[6:7], v[6:7], v[60:61] op_sel_hi:[1,0]
	v_pk_mul_f32 v[2:3], v[2:3], v[60:61] op_sel_hi:[1,0]
	s_nop 0
	v_pk_mul_f32 v[28:29], v[112:113], v[36:37]
	s_nop 0
	v_pk_mul_f32 v[32:33], v[116:117], v[40:41]
	v_pk_mul_f32 v[30:31], v[114:115], v[38:39]
	v_pk_mul_f32 v[34:35], v[118:119], v[42:43]
	v_cvt_pk_bf16_f32 v28, v28, v29
	v_cvt_pk_bf16_f32 v29, v30, v31
	v_cvt_pk_bf16_f32 v30, v32, v33
	v_cvt_pk_bf16_f32 v31, v34, v35
	global_store_dwordx4 v[18:19], v[28:31], off offset:1024
	s_nop 0
	s_nop 0
	s_nop 0
	v_pk_mul_f32 v[36:37], v[44:45], v[60:61] op_sel_hi:[1,0]
	v_pk_mul_f32 v[38:39], v[48:49], v[60:61] op_sel_hi:[1,0]
	v_pk_mul_f32 v[40:41], v[46:47], v[60:61] op_sel_hi:[1,0]
	v_pk_mul_f32 v[42:43], v[50:51], v[60:61] op_sel_hi:[1,0]
	s_nop 0
	v_pk_mul_f32 v[28:29], v[120:121], v[36:37]
	s_nop 0
	v_pk_mul_f32 v[32:33], v[124:125], v[38:39]
	v_pk_mul_f32 v[30:31], v[122:123], v[40:41]
	v_pk_mul_f32 v[34:35], v[126:127], v[42:43]
	v_cvt_pk_bf16_f32 v28, v28, v29
	v_cvt_pk_bf16_f32 v29, v30, v31
	v_cvt_pk_bf16_f32 v30, v32, v33
	v_cvt_pk_bf16_f32 v31, v34, v35
	global_store_dwordx4 v[18:19], v[28:31], off offset:2048
	s_nop 0
	s_nop 0
	s_nop 0
	s_nop 0
	v_pk_mul_f32 v[4:5], v[128:129], v[4:5]
	s_nop 0
	v_pk_mul_f32 v[28:29], v[132:133], v[0:1]
	v_pk_mul_f32 v[6:7], v[130:131], v[6:7]
	v_pk_mul_f32 v[30:31], v[134:135], v[2:3]
	v_cvt_pk_bf16_f32 v0, v4, v5
	v_cvt_pk_bf16_f32 v1, v6, v7
	v_cvt_pk_bf16_f32 v2, v28, v29
	v_cvt_pk_bf16_f32 v3, v30, v31
	global_store_dwordx4 v[18:19], v[0:3], off offset:3072
	v_lshl_add_u64 v[18:19], v[18:19], 0, s[4:5]
	s_branch .LBB0_167

; __device__ __forceinline__ void ph_final(const Ctx& c) {
;     const bf16* Ys = WSP(bf16, WS_KV); const float* X = WSP(float, WS_XA); const float* g = c.in[3];
;     const int gw = c.bid * NWAVE + c.wave, nw = c.G * NWAVE;
;     for (int row = gw; row < T_; row += nw) {
;         float v[32]; row_load32_nt(X + (size_t)row * D_, c.lane, v);
;         row_add_bf16_nt(Ys + (size_t)(2 * row) * D_, c.lane, v); row_add_bf16_nt(Ys + (size_t)(2 * row + 1) * D_, c.lane, v);
;     ...
;         for (int cch = 0; cch < 4; ++cch) { const f32x4 ga = *(const f32x4*)(g + cch * 512 + c.lane * 8), gb = *(const f32x4*)(g + cch * 512 + c.lane * 8 + 4);
.LBB0_2595:
	v_readlane_b32 s0, v254, 5
	v_readlane_b32 s1, v254, 6
	s_cmp_lt_i32 s0, 18
	s_cselect_b64 s[0:1], -1, 0
	s_and_b64 s[0:1], s[0:1], s[4:5]
	s_andn2_b64 vcc, exec, s[0:1]
	s_cbranch_vccnz .LBB0_2599
	s_lshl_b32 s0, s2, 3
	v_readlane_b32 s1, v254, 46
	s_add_i32 s0, s0, s1
	s_cmpk_gt_i32 s0, 0x3fff
	s_cbranch_scc1 .LBB0_2599
	v_mbcnt_lo_u32_b32 v0, -1, 0
	v_mbcnt_hi_u32_b32 v0, -1, v0
	v_and_b32_e32 v1, 64, v0
	v_add_u32_e32 v1, 64, v1
	v_xor_b32_e32 v3, 32, v0
	v_cmp_lt_i32_e32 vcc, v3, v1
	s_lshl_b32 s1, s2, 4
	v_readlane_b32 s2, v254, 46
	v_cndmask_b32_e32 v3, v0, v3, vcc
	v_lshlrev_b32_e32 v20, 2, v3
	v_xor_b32_e32 v3, 16, v0
	v_cmp_lt_i32_e32 vcc, v3, v1
	s_mov_b64 s[6:7], 0x59500000
	s_lshl_b32 s2, s2, 1
	v_cndmask_b32_e32 v3, v0, v3, vcc
	v_lshlrev_b32_e32 v21, 2, v3
	v_xor_b32_e32 v3, 8, v0
	v_cmp_lt_i32_e32 vcc, v3, v1
	s_add_i32 s2, s1, s2
	s_ashr_i32 s1, s0, 31
	v_cndmask_b32_e32 v3, v0, v3, vcc
	v_lshlrev_b32_e32 v22, 2, v3
	v_xor_b32_e32 v3, 4, v0
	v_cmp_lt_i32_e32 vcc, v3, v1
	s_lshl_b32 s4, s96, 3
	s_lshl_b32 s20, s96, 4
	v_cndmask_b32_e32 v3, v0, v3, vcc
	v_lshlrev_b32_e32 v23, 2, v3
	v_xor_b32_e32 v3, 2, v0
	v_cmp_lt_i32_e32 vcc, v3, v1
	s_lshl_b64 s[10:11], s[0:1], 13
	v_readlane_b32 s12, v254, 0
	v_cndmask_b32_e32 v3, v0, v3, vcc
	v_lshlrev_b32_e32 v24, 2, v3
	v_xor_b32_e32 v3, 1, v0
	v_cmp_lt_i32_e32 vcc, v3, v1
	v_readlane_b32 s14, v254, 2
	v_readlane_b32 s13, v254, 1
	v_cndmask_b32_e32 v0, v0, v3, vcc
	v_lshlrev_b32_e32 v25, 2, v0
	v_lshlrev_b32_e32 v0, 3, v2
	v_ashrrev_i32_e32 v1, 31, v0
	v_lshl_add_u64 v[2:3], v[0:1], 1, s[46:47]
	v_lshlrev_b64 v[10:11], 2, v[0:1]
	v_lshl_add_u64 v[8:9], v[2:3], 0, s[6:7]
	v_lshl_add_u64 v[12:13], s[54:55], 0, v[10:11]
	s_mov_b64 s[6:7], 0x1000
	v_lshl_add_u64 v[14:15], v[12:13], 0, s[6:7]
	s_mov_b64 s[6:7], 0x1800
	v_lshl_add_u64 v[16:17], v[12:13], 0, s[6:7]
	s_add_u32 s6, s46, s10
	s_addc_u32 s7, s47, s11
	s_ashr_i32 s5, s4, 31
	s_lshl_b64 s[8:9], s[4:5], 13
	v_readlane_b32 s15, v254, 3
	s_add_u32 s10, s14, s10
	s_addc_u32 s11, s15, s11
	s_mov_b64 s[12:13], 0x3b500000
	s_mov_b64 s[14:15], 0x3b500800
	s_mov_b64 s[16:17], 0x3b501000
	s_mov_b64 s[18:19], 0x3b501800
	v_mov_b32_e32 v26, 0x358637bd
	s_mov_b32 s1, 0x800000
	s_movk_i32 s5, 0x1000
	global_load_dwordx4 v[112:115], v[12:13], off offset:16
	global_load_dwordx4 v[116:119], v[12:13], off
	global_load_dwordx4 v[120:123], v[12:13], off offset:2048
	global_load_dwordx4 v[124:127], v[12:13], off offset:2064
	global_load_dwordx4 v[128:131], v[14:15], off
	global_load_dwordx4 v[132:135], v[14:15], off offset:16
	global_load_dwordx4 v[136:139], v[16:17], off
	global_load_dwordx4 v[140:143], v[16:17], off offset:16
	s_waitcnt vmcnt(0)
.LBB0_2598:
	s_ashr_i32 s3, s2, 31
	v_lshl_add_u64 v[60:61], s[6:7], 0, v[10:11]
	s_lshl_b64 s[24:25], s[2:3], 12
	v_add_co_u32_e32 v64, vcc, 0x3b500000, v60
	v_lshl_add_u64 v[68:69], v[8:9], 0, s[24:25]
	s_add_i32 s22, s2, 1
	s_nop 0
	s_nop 0
	v_lshl_add_u64 v[62:63], v[60:61], 0, s[12:13]
	v_lshl_add_u64 v[66:67], v[60:61], 0, s[14:15]
	v_addc_co_u32_e32 v65, vcc, 0, v61, vcc
	global_load_dwordx4 v[28:31], v[68:69], off nt
	global_load_dwordx4 v[32:35], v[68:69], off offset:1024 nt
	global_load_dwordx4 v[36:39], v[68:69], off offset:2048 nt
	global_load_dwordx4 v[40:43], v[68:69], off offset:3072 nt
	global_load_dwordx4 v[44:47], v[64:65], off nt
	global_load_dwordx4 v[48:51], v[62:63], off offset:16 nt
	global_load_dwordx4 v[52:55], v[64:65], off offset:2048 nt
	global_load_dwordx4 v[56:59], v[66:67], off offset:16 nt
	s_ashr_i32 s23, s22, 31
	s_lshl_b64 s[22:23], s[22:23], 12
	v_add_co_u32_e32 v96, vcc, 0x3b501000, v60
	v_lshl_add_u64 v[98:99], v[8:9], 0, s[22:23]
	v_lshl_add_u64 v[92:93], v[60:61], 0, s[16:17]
	v_lshl_add_u64 v[94:95], v[60:61], 0, s[18:19]
	v_addc_co_u32_e32 v97, vcc, 0, v61, vcc
	global_load_dwordx4 v[60:63], v[98:99], off nt
	global_load_dwordx4 v[64:67], v[98:99], off offset:1024 nt
	global_load_dwordx4 v[68:71], v[96:97], off nt
	global_load_dwordx4 v[72:75], v[98:99], off offset:2048 nt
	global_load_dwordx4 v[76:79], v[92:93], off offset:16 nt
	global_load_dwordx4 v[80:83], v[96:97], off offset:2048 nt
	global_load_dwordx4 v[84:87], v[98:99], off offset:3072 nt
	global_load_dwordx4 v[88:91], v[94:95], off offset:16 nt
	v_lshl_add_u64 v[18:19], s[10:11], 0, v[10:11]
	s_add_i32 s0, s0, s4
	s_add_i32 s2, s2, s20
	s_add_u32 s6, s6, s8
	s_addc_u32 s7, s7, s9
	s_add_u32 s10, s10, s8
	s_addc_u32 s11, s11, s9
	s_cmpk_lt_i32 s0, 0x4000
	s_waitcnt vmcnt(0)
; __device__ __forceinline__ void row_add_bf16_nt(const bf16* __restrict__ p, int lane, float (&v)[32]) {
; #pragma unroll
;     for (int cch = 0; cch < 4; ++cch) { const u32x4 w = __builtin_nontemporal_load((const u32x4*)(p + cch * 512 + lane * 8)); float f[8]; unpack8(w, f);
; #pragma unroll
;         for (int j = 0; j < 8; ++j) v[cch * 8 + j] += f[j]; }
; }
; __device__ __forceinline__ float row_rstd(const float (&v)[32]) {
;     float ss = 0.f;
; #pragma unroll
;     for (int j = 0; j < 32; ++j) ss += v[j] * v[j];
	v_lshlrev_b32_e32 v92, 16, v28
	v_and_b32_e32 v93, 0xffff0000, v28
	v_lshlrev_b32_e32 v28, 16, v29
	v_and_b32_e32 v29, 0xffff0000, v29
	v_lshlrev_b32_e32 v94, 16, v30
	v_and_b32_e32 v95, 0xffff0000, v30
	v_pk_add_f32 v[44:45], v[44:45], v[92:93]
	v_lshlrev_b32_e32 v30, 16, v31
	v_and_b32_e32 v31, 0xffff0000, v31
	v_lshlrev_b32_e32 v96, 16, v32
	v_lshlrev_b32_e32 v92, 16, v60
	v_and_b32_e32 v93, 0xffff0000, v60
	v_and_b32_e32 v97, 0xffff0000, v32
	v_pk_add_f32 v[28:29], v[46:47], v[28:29]
	v_lshlrev_b32_e32 v46, 16, v61
	v_and_b32_e32 v47, 0xffff0000, v61
	v_pk_add_f32 v[48:49], v[48:49], v[94:95]
	v_lshlrev_b32_e32 v60, 16, v62
	v_and_b32_e32 v61, 0xffff0000, v62
	v_pk_add_f32 v[44:45], v[44:45], v[92:93]
	v_pk_add_f32 v[30:31], v[50:51], v[30:31]
	v_lshlrev_b32_e32 v50, 16, v63
	v_and_b32_e32 v51, 0xffff0000, v63
	v_pk_add_f32 v[52:53], v[52:53], v[96:97]
	v_lshlrev_b32_e32 v62, 16, v64
	v_and_b32_e32 v63, 0xffff0000, v64
	v_pk_add_f32 v[28:29], v[28:29], v[46:47]
	v_pk_add_f32 v[46:47], v[48:49], v[60:61]
	v_pk_mul_f32 v[60:61], v[44:45], v[44:45]
	v_lshlrev_b32_e32 v32, 16, v33
	v_and_b32_e32 v33, 0xffff0000, v33
	v_lshlrev_b32_e32 v98, 16, v34
	v_and_b32_e32 v99, 0xffff0000, v34
	v_pk_add_f32 v[48:49], v[52:53], v[62:63]
	v_pk_mul_f32 v[62:63], v[28:29], v[28:29]
	v_add_f32_e32 v27, v60, v61
	v_pk_add_f32 v[32:33], v[54:55], v[32:33]
	v_lshlrev_b32_e32 v54, 16, v65
	v_and_b32_e32 v55, 0xffff0000, v65
	v_pk_add_f32 v[56:57], v[56:57], v[98:99]
	v_lshlrev_b32_e32 v64, 16, v66
	v_and_b32_e32 v65, 0xffff0000, v66
	v_add_f32_e32 v27, v62, v27
	v_lshlrev_b32_e32 v34, 16, v35
	v_and_b32_e32 v35, 0xffff0000, v35
	v_lshlrev_b32_e32 v100, 16, v36
	v_and_b32_e32 v101, 0xffff0000, v36
	v_pk_add_f32 v[30:31], v[30:31], v[50:51]
	v_pk_add_f32 v[50:51], v[56:57], v[64:65]
	v_pk_mul_f32 v[64:65], v[46:47], v[46:47]
	v_add_f32_e32 v27, v63, v27
	v_pk_add_f32 v[34:35], v[58:59], v[34:35]
	v_lshlrev_b32_e32 v58, 16, v67
	v_and_b32_e32 v59, 0xffff0000, v67
	v_pk_add_f32 v[66:67], v[68:69], v[100:101]
	v_lshlrev_b32_e32 v68, 16, v72
	v_and_b32_e32 v69, 0xffff0000, v72
	v_add_f32_e32 v27, v64, v27
	v_pk_add_f32 v[52:53], v[66:67], v[68:69]
	v_pk_mul_f32 v[66:67], v[30:31], v[30:31]
	v_add_f32_e32 v27, v65, v27
	v_add_f32_e32 v27, v66, v27
	v_lshlrev_b32_e32 v36, 16, v37
	v_and_b32_e32 v37, 0xffff0000, v37
	v_pk_mul_f32 v[68:69], v[48:49], v[48:49]
	v_add_f32_e32 v27, v67, v27
	v_pk_add_f32 v[36:37], v[70:71], v[36:37]
	v_lshlrev_b32_e32 v70, 16, v73
	v_and_b32_e32 v71, 0xffff0000, v73
	v_pk_add_f32 v[32:33], v[32:33], v[54:55]
	v_add_f32_e32 v27, v68, v27
	v_lshlrev_b32_e32 v102, 16, v38
	v_and_b32_e32 v103, 0xffff0000, v38
	v_pk_add_f32 v[36:37], v[36:37], v[70:71]
	v_pk_mul_f32 v[70:71], v[32:33], v[32:33]
	v_add_f32_e32 v27, v69, v27
	v_pk_add_f32 v[72:73], v[76:77], v[102:103]
	v_lshlrev_b32_e32 v76, 16, v74
	v_and_b32_e32 v77, 0xffff0000, v74
	v_add_f32_e32 v27, v70, v27
	v_lshlrev_b32_e32 v38, 16, v39
	v_and_b32_e32 v39, 0xffff0000, v39
	v_pk_add_f32 v[54:55], v[72:73], v[76:77]
	v_pk_mul_f32 v[72:73], v[50:51], v[50:51]
	v_add_f32_e32 v27, v71, v27
	v_pk_add_f32 v[38:39], v[78:79], v[38:39]
	v_lshlrev_b32_e32 v74, 16, v75
	v_and_b32_e32 v75, 0xffff0000, v75
	v_pk_add_f32 v[34:35], v[34:35], v[58:59]
	v_add_f32_e32 v27, v72, v27
	v_pk_add_f32 v[38:39], v[38:39], v[74:75]
	v_pk_mul_f32 v[74:75], v[34:35], v[34:35]
	v_add_f32_e32 v27, v73, v27
	v_add_f32_e32 v27, v74, v27
	v_lshlrev_b32_e32 v104, 16, v40
	v_and_b32_e32 v105, 0xffff0000, v40
	v_pk_mul_f32 v[76:77], v[52:53], v[52:53]
	v_add_f32_e32 v27, v75, v27
	v_pk_add_f32 v[78:79], v[80:81], v[104:105]
	v_lshlrev_b32_e32 v80, 16, v84
	v_and_b32_e32 v81, 0xffff0000, v84
	v_add_f32_e32 v27, v76, v27
	v_pk_add_f32 v[56:57], v[78:79], v[80:81]
	v_pk_mul_f32 v[78:79], v[36:37], v[36:37]
	v_add_f32_e32 v27, v77, v27
	v_add_f32_e32 v27, v78, v27
	v_lshlrev_b32_e32 v40, 16, v41
	v_and_b32_e32 v41, 0xffff0000, v41
	v_pk_mul_f32 v[80:81], v[54:55], v[54:55]
	v_add_f32_e32 v27, v79, v27
	v_pk_add_f32 v[40:41], v[82:83], v[40:41]
	v_lshlrev_b32_e32 v82, 16, v85
	v_and_b32_e32 v83, 0xffff0000, v85
	v_add_f32_e32 v27, v80, v27
	v_lshlrev_b32_e32 v106, 16, v42
	v_and_b32_e32 v107, 0xffff0000, v42
	v_pk_add_f32 v[40:41], v[40:41], v[82:83]
	v_pk_mul_f32 v[82:83], v[38:39], v[38:39]
	v_add_f32_e32 v27, v81, v27
	v_pk_add_f32 v[84:85], v[88:89], v[106:107]
	v_lshlrev_b32_e32 v88, 16, v86
	v_and_b32_e32 v89, 0xffff0000, v86
	v_add_f32_e32 v27, v82, v27
	v_lshlrev_b32_e32 v42, 16, v43
	v_and_b32_e32 v43, 0xffff0000, v43
	v_pk_add_f32 v[58:59], v[84:85], v[88:89]
	v_pk_mul_f32 v[84:85], v[56:57], v[56:57]
	v_add_f32_e32 v27, v83, v27
	v_pk_add_f32 v[42:43], v[90:91], v[42:43]
	v_lshlrev_b32_e32 v86, 16, v87
	v_and_b32_e32 v87, 0xffff0000, v87
	v_add_f32_e32 v27, v84, v27
	v_pk_add_f32 v[42:43], v[42:43], v[86:87]
	v_pk_mul_f32 v[86:87], v[40:41], v[40:41]
	v_add_f32_e32 v27, v85, v27
	v_add_f32_e32 v27, v86, v27
	v_pk_mul_f32 v[88:89], v[58:59], v[58:59]
	v_add_f32_e32 v27, v87, v27
	v_add_f32_e32 v27, v88, v27
	v_pk_mul_f32 v[90:91], v[42:43], v[42:43]
	v_add_f32_e32 v27, v89, v27
	v_add_f32_e32 v27, v90, v27
	v_add_f32_e32 v27, v91, v27
	ds_bpermute_b32 v60, v20, v27
	s_waitcnt lgkmcnt(0)
; __device__ __forceinline__ float wave_sum(float v) {
; #pragma unroll
;     for (int o = 32; o >= 1; o >>= 1) v += __shfl_xor(v, o);
;     return v;
; __device__ __forceinline__ void ph_final(const Ctx& c) {
;     ...
;         const float r = row_rstd(v);
; #pragma unroll
;         for (int cch = 0; cch < 4; ++cch) { const f32x4 ga = *(const f32x4*)(g + cch * 512 + c.lane * 8), gb = *(const f32x4*)(g + cch * 512 + c.lane * 8 + 4);
;             *(f32x4*)(c.out + (size_t)row * D_ + cch * 512 + c.lane * 8) = (f32x4){v[cch * 8] * r * ga[0], v[cch * 8 + 1] * r * ga[1], v[cch * 8 + 2] * r * ga[2], v[cch * 8 + 3] * r * ga[3]};
;             *(f32x4*)(c.out + (size_t)row * D_ + cch * 512 + c.lane * 8 + 4) = (f32x4){v[cch * 8 + 4] * r * gb[0], v[cch * 8 + 5] * r * gb[1], v[cch * 8 + 6] * r * gb[2], v[cch * 8 + 7] * r * gb[3]}; }
	v_add_f32_e32 v27, v27, v60
	ds_bpermute_b32 v60, v21, v27
	s_waitcnt lgkmcnt(0)
	v_add_f32_e32 v27, v27, v60
	ds_bpermute_b32 v60, v22, v27
	s_waitcnt lgkmcnt(0)
	v_add_f32_e32 v27, v27, v60
	ds_bpermute_b32 v60, v23, v27
	s_waitcnt lgkmcnt(0)
	v_add_f32_e32 v27, v27, v60
	ds_bpermute_b32 v60, v24, v27
	s_waitcnt lgkmcnt(0)
	v_add_f32_e32 v27, v27, v60
	ds_bpermute_b32 v60, v25, v27
	s_waitcnt lgkmcnt(0)
	v_add_f32_e32 v27, v27, v60
	v_fmamk_f32 v27, v27, 0x3a000000, v26
	v_mul_f32_e32 v60, 0x4b800000, v27
	v_cmp_gt_f32_e32 vcc, s1, v27
	s_nop 1
	v_cndmask_b32_e32 v27, v27, v60, vcc
	v_rsq_f32_e32 v27, v27
	s_nop 0
	v_mul_f32_e32 v60, 0x45800000, v27
	v_cndmask_b32_e32 v60, v27, v60, vcc
	v_pk_mul_f32 v[44:45], v[44:45], v[60:61] op_sel_hi:[1,0]
	v_pk_mul_f32 v[28:29], v[28:29], v[60:61] op_sel_hi:[1,0]
	v_pk_mul_f32 v[46:47], v[46:47], v[60:61] op_sel_hi:[1,0]
	v_pk_mul_f32 v[30:31], v[30:31], v[60:61] op_sel_hi:[1,0]
	v_pk_mul_f32 v[6:7], v[118:119], v[28:29]
	v_pk_mul_f32 v[4:5], v[116:117], v[44:45]
	v_pk_mul_f32 v[2:3], v[114:115], v[30:31]
	v_pk_mul_f32 v[0:1], v[112:113], v[46:47]
	global_store_dwordx4 v[18:19], v[4:7], off
	global_store_dwordx4 v[18:19], v[0:3], off offset:16
	s_nop 0
	s_nop 0
	s_nop 0
	v_pk_mul_f32 v[28:29], v[32:33], v[60:61] op_sel_hi:[1,0]
	v_pk_mul_f32 v[30:31], v[48:49], v[60:61] op_sel_hi:[1,0]
	v_pk_mul_f32 v[32:33], v[34:35], v[60:61] op_sel_hi:[1,0]
	v_pk_mul_f32 v[34:35], v[50:51], v[60:61] op_sel_hi:[1,0]
	s_nop 0
	v_pk_mul_f32 v[0:1], v[120:121], v[30:31]
	v_pk_mul_f32 v[2:3], v[122:123], v[28:29]
	s_nop 0
	v_pk_mul_f32 v[4:5], v[124:125], v[34:35]
	v_pk_mul_f32 v[6:7], v[126:127], v[32:33]
	global_store_dwordx4 v[18:19], v[0:3], off offset:2048
	global_store_dwordx4 v[18:19], v[4:7], off offset:2064
	s_nop 0
	s_nop 0
	s_nop 0
	v_add_co_u32_e32 v18, vcc, s5, v18
	v_pk_mul_f32 v[28:29], v[36:37], v[60:61] op_sel_hi:[1,0]
	v_pk_mul_f32 v[30:31], v[52:53], v[60:61] op_sel_hi:[1,0]
	v_addc_co_u32_e32 v19, vcc, 0, v19, vcc
	v_pk_mul_f32 v[32:33], v[38:39], v[60:61] op_sel_hi:[1,0]
	v_pk_mul_f32 v[34:35], v[54:55], v[60:61] op_sel_hi:[1,0]
	s_nop 0
	v_pk_mul_f32 v[0:1], v[128:129], v[30:31]
	v_pk_mul_f32 v[2:3], v[130:131], v[28:29]
	s_nop 0
	v_pk_mul_f32 v[4:5], v[132:133], v[34:35]
	v_pk_mul_f32 v[6:7], v[134:135], v[32:33]
	global_store_dwordx4 v[18:19], v[0:3], off
	global_store_dwordx4 v[18:19], v[4:7], off offset:16
	s_nop 0
	s_nop 0
	s_nop 0
	v_pk_mul_f32 v[28:29], v[40:41], v[60:61] op_sel_hi:[1,0]
	v_pk_mul_f32 v[30:31], v[56:57], v[60:61] op_sel_hi:[1,0]
	v_pk_mul_f32 v[32:33], v[42:43], v[60:61] op_sel_hi:[1,0]
	v_pk_mul_f32 v[34:35], v[58:59], v[60:61] op_sel_hi:[1,0]
	s_nop 0
	v_pk_mul_f32 v[0:1], v[136:137], v[30:31]
	v_pk_mul_f32 v[2:3], v[138:139], v[28:29]
	s_nop 0
	v_pk_mul_f32 v[4:5], v[140:141], v[34:35]
	v_pk_mul_f32 v[6:7], v[142:143], v[32:33]
	global_store_dwordx4 v[18:19], v[0:3], off offset:2048
	global_store_dwordx4 v[18:19], v[4:7], off offset:2064
	s_cbranch_scc1 .LBB0_2598
